# step-1 vmcnt waits relaxed to exact steady-state counts (19/18/17/16), first-iteration guard
# speedup vs baseline: 1.0302x; 1.0302x over previous
.LBB1_8:
	s_add_i32 s50, s41, 5
	s_lshr_b32 s38, s50, 2
	s_add_i32 s38, s38, s44
	s_lshl_b32 s38, s38, 17
	s_add_i32 s47, s20, 0x8000
	s_add_i32 s48, s41, 9
	s_and_b32 s38, s38, 0xe0000
	s_and_b32 s47, s47, 0xc000
	s_lshr_b32 s49, s48, 2
	s_or_b32 s38, s38, s47
	s_and_b32 s47, s48, 3
	s_add_i32 s49, s49, s44
	v_lshl_add_u64 v[150:151], v[194:195], 0, s[38:39]
	s_min_u32 s38, s47, s46
	s_lshl_b32 s49, s49, 10
	s_and_b32 s49, s49, 0x1c00
	s_lshl_b32 s38, s38, 18
	s_add_i32 s21, s41, 3
	v_add_co_u32_e32 v146, vcc, s45, v150
	s_or_b32 s38, s49, s38
	s_nop 0
	v_addc_co_u32_e32 v147, vcc, 0, v151, vcc
	s_cmp_lt_u32 s21, 26
	v_add_co_u32_e32 v152, vcc, s40, v150
	s_cselect_b32 s49, 0, 2.0
	s_nop 0
	v_addc_co_u32_e32 v153, vcc, 0, v151, vcc
	v_add_u32_e32 v154, s49, v197
	v_add_u32_e32 v155, s49, v198
	global_load_dwordx4 v[158:161], v[146:147], off offset:-4096
	s_nop 0
	global_load_dwordx4 v[146:149], v[146:147], off
	s_nop 0
	global_load_dwordx4 v[166:169], v[150:151], off
	s_nop 0
	global_load_dwordx4 v[150:153], v[152:153], off
	s_nop 0
	buffer_load_dwordx4 v[174:177], v154, s[4:7], s38 offen sc0 nt sc1
	buffer_load_dwordx4 v[170:173], v155, s[4:7], s38 offen sc0 nt sc1
	v_add_u32_e32 v154, s49, v199
	v_add_u32_e32 v155, s49, v200
	buffer_load_dwordx4 v[162:165], v154, s[4:7], s38 offen sc0 nt sc1
	s_nop 0
	buffer_load_dwordx4 v[154:157], v155, s[4:7], s38 offen sc0 nt sc1
	s_and_b32 s51, s21, 3
	s_bfe_u32 s38, s21, 0x10002
	s_lshl_b32 s49, s51, 6
	v_lshl_or_b32 v207, s38, 16, v204
	v_xor_b32_e32 v215, s49, v203
	v_add_u32_e32 v226, v207, v215
	ds_read_b128 v[208:211], v226
	ds_read_b128 v[216:219], v226 offset:16384
	ds_read_b128 v[220:223], v226 offset:32768
	ds_read_b128 v[226:229], v226 offset:49152
	v_lshl_add_u32 v240, s38, 14, v206
	v_add_u32_e32 v230, v240, v215
	ds_read_b128 v[230:233], v230
	s_add_i32 s38, s20, 0x10000
	s_and_b32 s38, s38, 0x10000
	s_lshl_b32 s49, s51, 14
	s_or_b32 s38, s38, s49
	s_lshl_b32 s53, s51, 2
	s_cmp_lg_u32 s41, -3
	s_cbranch_scc1 .Lsteady_w1
	s_waitcnt vmcnt(9)
.Lsteady_w1:
	s_waitcnt vmcnt(19)
	v_cvt_pk_f16_f32 v234, v142, v143
	v_cvt_pk_f16_f32 v235, v144, v145
	v_or_b32_e32 v236, s38, v202
	ds_write_b64 v236, v[234:235]
	v_bfe_u32 v234, v205, s53, 1
	v_cmp_eq_u32_e32 vcc, 0, v234
	v_lshrrev_b32_e32 v241, s53, v205
	s_waitcnt vmcnt(18)
	v_cvt_pk_f16_f32 v236, v138, v139
	v_cndmask_b32_e64 v234, 1.0, 0, vcc
	v_pk_fma_f32 v[142:143], v[234:235], v[142:143], 0 op_sel_hi:[0,1,0]
	v_cvt_pk_f16_f32 v237, v140, v141
	v_or_b32_e32 v235, s38, v201
	ds_write_b64 v235, v[236:237] offset:4096
	v_and_b32_e32 v235, 2, v241
	v_cmp_eq_u32_e32 vcc, 0, v235
	s_add_i32 s52, s41, 7
	s_nop 0
	v_cndmask_b32_e64 v236, 1.0, 0, vcc
	v_pk_fma_f32 v[238:239], v[236:237], v[138:139], v[142:143] op_sel_hi:[0,1,1]
	v_xor_b32_e32 v215, 32, v215
	s_waitcnt lgkmcnt(6)
	v_mfma_f32_32x32x16_f16 v[2:17], v[118:121], v[208:211], v[2:17]
	v_add_u32_e32 v207, v207, v215
	v_fma_f32 v138, v234, v144, 0
	v_fma_f32 v139, v234, v145, 0
	s_waitcnt lgkmcnt(5)
	v_mfma_f32_32x32x16_f16 v[34:49], v[118:121], v[216:219], v[34:49]
	s_waitcnt lgkmcnt(4)
	v_mfma_f32_32x32x16_f16 v[50:65], v[118:121], v[220:223], v[50:65]
	v_fma_f32 v220, v236, v140, v138
	v_fma_f32 v221, v236, v141, v139
	v_add_u32_e32 v138, v240, v215
	s_waitcnt lgkmcnt(3)
	v_mfma_f32_32x32x16_f16 v[18:33], v[118:121], v[226:229], v[18:33]
	ds_read_b128 v[118:121], v207
	ds_read_b128 v[142:145], v207 offset:16384
	ds_read_b128 v[208:211], v207 offset:32768
	ds_read_b128 v[216:219], v207 offset:49152
	ds_read_b128 v[138:141], v138
	s_waitcnt lgkmcnt(7)
	v_mfma_f32_32x32x16_f16 v[66:81], v[114:117], v[230:233], v[66:81]
	s_bfe_u32 s38, s52, 0x10002
	s_lshl_b32 s53, s38, 16
	s_or_b32 s49, s53, s49
	s_waitcnt vmcnt(17)
	v_cvt_pk_f16_f32 v114, v134, v135
	v_cvt_pk_f16_f32 v115, v136, v137
	v_or_b32_e32 v116, s49, v202
	ds_write_b64 v116, v[114:115] offset:8192
	v_and_b32_e32 v114, 4, v241
	v_cmp_eq_u32_e32 vcc, 0, v114
	s_lshl_b32 s38, s38, 14
	s_nop 0
	v_cndmask_b32_e64 v114, 1.0, 0, vcc
	v_pk_fma_f32 v[116:117], v[114:115], v[134:135], v[238:239] op_sel_hi:[0,1,1]
	v_pk_fma_f32 v[114:115], v[114:115], v[136:137], v[220:221] op_sel_hi:[0,1,1]
	s_waitcnt vmcnt(16)
	v_cvt_pk_f16_f32 v134, v130, v131
	v_cvt_pk_f16_f32 v135, v132, v133
	v_or_b32_e32 v136, s49, v201
	s_lshl_b32 s49, s51, 12
	ds_write_b64 v136, v[134:135] offset:12288
	v_and_b32_e32 v134, 8, v241
	s_or_b32 s38, s38, s49
	v_cmp_eq_u32_e32 vcc, 0, v134
	s_bitcmp0_b32 s21, 0
	s_nop 0
	v_cndmask_b32_e64 v134, 1.0, 0, vcc
	s_cselect_b64 vcc, -1, 0
	v_pk_fma_f32 v[116:117], v[134:135], v[130:131], v[116:117] op_sel_hi:[0,1,1]
	v_pk_fma_f32 v[114:115], v[134:135], v[132:133], v[114:115] op_sel_hi:[0,1,1]
	v_cndmask_b32_e32 v207, v201, v202, vcc
	v_cvt_pk_f16_f32 v116, v116, v117
	v_cvt_pk_f16_f32 v117, v114, v115
	v_or_b32_e32 v114, s38, v207
	v_or_b32_e32 v114, 0x20000, v114
	ds_write_b64 v114, v[116:117]
	s_waitcnt lgkmcnt(7)
	v_mfma_f32_32x32x16_f16 v[2:17], v[90:93], v[118:121], v[2:17]
	s_waitcnt lgkmcnt(6)
	v_mfma_f32_32x32x16_f16 v[34:49], v[90:93], v[142:145], v[34:49]
	s_waitcnt lgkmcnt(5)
	v_mfma_f32_32x32x16_f16 v[50:65], v[90:93], v[208:211], v[50:65]
	s_waitcnt lgkmcnt(4)
	v_mfma_f32_32x32x16_f16 v[18:33], v[90:93], v[216:219], v[18:33]
	s_waitcnt lgkmcnt(3)
	v_mfma_f32_32x32x16_f16 v[66:81], v[98:101], v[138:141], v[66:81]
	s_cmp_lg_u32 s51, 3
	s_cbranch_scc1 .LBB1_10
	s_waitcnt lgkmcnt(0)
	s_barrier
.LBB1_10:
	s_add_i32 s38, s41, 6
	s_lshr_b32 s38, s38, 2
	s_add_i32 s38, s38, s44
	s_lshl_b32 s38, s38, 17
	s_add_i32 s49, s20, 0xc000
	s_and_b32 s38, s38, 0xe0000
	s_and_b32 s53, s49, 0xc000
	s_or_b32 s38, s38, s53
	v_lshl_add_u64 v[90:91], v[194:195], 0, s[38:39]
	s_add_i32 s38, s41, 10
	s_and_b32 s53, s38, 3
	s_lshr_b32 s38, s38, 2
	s_add_i32 s38, s38, s44
	v_add_co_u32_e32 v92, vcc, 0x1000, v90
	s_min_u32 s53, s53, s46
	s_lshl_b32 s38, s38, 10
	v_addc_co_u32_e32 v93, vcc, 0, v91, vcc
	s_and_b32 s38, s38, 0x1c00
	s_lshl_b32 s53, s53, 18
	global_load_dwordx4 v[118:121], v[90:91], off
	global_load_dwordx4 v[114:117], v[92:93], off
	v_add_co_u32_e32 v92, vcc, 0x2000, v90
	s_or_b32 s38, s38, s53
	s_nop 0
	v_addc_co_u32_e32 v93, vcc, 0, v91, vcc
	s_cmp_lt_u32 s21, 25
	v_add_co_u32_e32 v98, vcc, 0x3000, v90
	s_cselect_b32 s53, 0, 2.0
	s_nop 0
	v_addc_co_u32_e32 v99, vcc, 0, v91, vcc
	v_add_u32_e32 v130, s53, v197
	v_add_u32_e32 v131, s53, v198
	global_load_dwordx4 v[90:93], v[92:93], off
	s_nop 0
	global_load_dwordx4 v[98:101], v[98:99], off
	s_nop 0
	buffer_load_dwordx4 v[142:145], v130, s[4:7], s38 offen sc0 nt sc1
	buffer_load_dwordx4 v[138:141], v131, s[4:7], s38 offen sc0 nt sc1
	v_add_u32_e32 v130, s53, v199
	v_add_u32_e32 v131, s53, v200
	buffer_load_dwordx4 v[134:137], v130, s[4:7], s38 offen sc0 nt sc1
	s_nop 0
	buffer_load_dwordx4 v[130:133], v131, s[4:7], s38 offen sc0 nt sc1
	s_add_i32 s38, s41, 4
	s_bfe_u32 s53, s38, 0x10002
	s_and_b32 s38, s38, 3
	s_lshl_b32 s54, s38, 6
	v_lshl_or_b32 v215, s53, 16, v204
	v_xor_b32_e32 v240, s54, v203
	v_add_u32_e32 v226, v215, v240
	ds_read_b128 v[208:211], v226
	ds_read_b128 v[216:219], v226 offset:16384
	ds_read_b128 v[220:223], v226 offset:32768
	ds_read_b128 v[226:229], v226 offset:49152
	v_lshl_add_u32 v241, s53, 14, v206
	v_add_u32_e32 v230, v241, v240
	ds_read_b128 v[230:233], v230
	s_add_i32 s53, s41, 8
	s_and_b32 s54, s53, 3
	s_add_i32 s55, s20, 0x14000
	s_and_b32 s55, s55, 0x10000
	s_lshl_b32 s56, s54, 14
	s_or_b32 s55, s55, s56
	s_lshl_b32 s57, s54, 2
	s_waitcnt vmcnt(19)
	v_cvt_pk_f16_f32 v234, v126, v127
	v_cvt_pk_f16_f32 v235, v128, v129
	v_or_b32_e32 v236, s55, v202
	ds_write_b64 v236, v[234:235]
	v_bfe_u32 v234, v205, s57, 1
	v_cmp_eq_u32_e32 vcc, 0, v234
	v_lshrrev_b32_e32 v242, s57, v205
	s_waitcnt vmcnt(18)
	v_cvt_pk_f16_f32 v236, v122, v123
	v_cndmask_b32_e64 v234, 1.0, 0, vcc
	v_pk_fma_f32 v[126:127], v[234:235], v[126:127], 0 op_sel_hi:[0,1,0]
	v_cvt_pk_f16_f32 v237, v124, v125
	v_or_b32_e32 v235, s55, v201
	ds_write_b64 v235, v[236:237] offset:4096
	v_and_b32_e32 v235, 2, v242
	v_cmp_eq_u32_e32 vcc, 0, v235
	s_nop 1
	v_cndmask_b32_e64 v236, 1.0, 0, vcc
	v_pk_fma_f32 v[238:239], v[236:237], v[122:123], v[126:127] op_sel_hi:[0,1,1]
	s_waitcnt lgkmcnt(4)
	v_mfma_f32_32x32x16_f16 v[50:65], v[102:105], v[220:223], v[50:65]
	v_xor_b32_e32 v222, 32, v240
	v_add_u32_e32 v215, v215, v222
	v_fma_f32 v122, v234, v128, 0
	v_fma_f32 v123, v234, v129, 0
	v_fma_f32 v220, v236, v124, v122
	v_fma_f32 v221, v236, v125, v123
	v_add_u32_e32 v122, v241, v222
	v_mfma_f32_32x32x16_f16 v[2:17], v[102:105], v[208:211], v[2:17]
	v_mfma_f32_32x32x16_f16 v[34:49], v[102:105], v[216:219], v[34:49]
	s_waitcnt lgkmcnt(3)
	v_mfma_f32_32x32x16_f16 v[18:33], v[102:105], v[226:229], v[18:33]
	ds_read_b128 v[102:105], v215
	ds_read_b128 v[126:129], v215 offset:16384
	ds_read_b128 v[208:211], v215 offset:32768
	ds_read_b128 v[216:219], v215 offset:49152
	ds_read_b128 v[122:125], v122
	s_waitcnt lgkmcnt(7)
	v_mfma_f32_32x32x16_f16 v[66:81], v[94:97], v[230:233], v[66:81]
	s_bfe_u32 s55, s53, 0x10002
	s_lshl_b32 s57, s55, 16
	s_or_b32 s56, s57, s56
	s_waitcnt vmcnt(17)
	v_cvt_pk_f16_f32 v94, v110, v111
	v_cvt_pk_f16_f32 v95, v112, v113
	v_or_b32_e32 v96, s56, v202
	ds_write_b64 v96, v[94:95] offset:8192
	v_and_b32_e32 v94, 4, v242
	v_cmp_eq_u32_e32 vcc, 0, v94
	s_lshl_b32 s55, s55, 14
	s_lshl_b32 s54, s54, 12
	v_cndmask_b32_e64 v94, 1.0, 0, vcc
	v_pk_fma_f32 v[96:97], v[94:95], v[110:111], v[238:239] op_sel_hi:[0,1,1]
	v_pk_fma_f32 v[94:95], v[94:95], v[112:113], v[220:221] op_sel_hi:[0,1,1]
	s_waitcnt vmcnt(16)
	v_cvt_pk_f16_f32 v110, v106, v107
	v_cvt_pk_f16_f32 v111, v108, v109
	v_or_b32_e32 v112, s56, v201
	ds_write_b64 v112, v[110:111] offset:12288
	v_and_b32_e32 v110, 8, v242
	v_cmp_eq_u32_e32 vcc, 0, v110
	s_or_b32 s54, s55, s54
	s_bitcmp0_b32 s53, 0
	v_cndmask_b32_e64 v110, 1.0, 0, vcc
	v_pk_fma_f32 v[96:97], v[110:111], v[106:107], v[96:97] op_sel_hi:[0,1,1]
	v_pk_fma_f32 v[94:95], v[110:111], v[108:109], v[94:95] op_sel_hi:[0,1,1]
	s_cselect_b64 vcc, -1, 0
	v_cvt_pk_f16_f32 v96, v96, v97
	v_cvt_pk_f16_f32 v97, v94, v95
	v_cndmask_b32_e32 v94, v201, v202, vcc
	v_or_b32_e32 v94, s54, v94
	v_or_b32_e32 v94, 0x20000, v94
	ds_write_b64 v94, v[96:97]
	s_waitcnt lgkmcnt(7)
	v_mfma_f32_32x32x16_f16 v[2:17], v[82:85], v[102:105], v[2:17]
	s_waitcnt lgkmcnt(6)
	v_mfma_f32_32x32x16_f16 v[34:49], v[82:85], v[126:129], v[34:49]
	s_waitcnt lgkmcnt(5)
	v_mfma_f32_32x32x16_f16 v[50:65], v[82:85], v[208:211], v[50:65]
	s_waitcnt lgkmcnt(4)
	v_mfma_f32_32x32x16_f16 v[18:33], v[82:85], v[216:219], v[18:33]
	s_waitcnt lgkmcnt(3)
	v_mfma_f32_32x32x16_f16 v[66:81], v[86:89], v[122:125], v[66:81]
	s_cmp_lg_u32 s38, 3
	s_cbranch_scc1 .LBB1_12
	s_waitcnt lgkmcnt(0)
	s_barrier
